# v39 + grid barrier: a waiting workgroup issues its acquire invalidate (L1) when the wait starts instead of after the flag
# speedup vs baseline: 1.0046x; 1.0046x over previous
.LBB0_1019:
	v_readlane_b32 s14, v250, 31
	v_readlane_b32 s15, v250, 32
	v_cvt_f32_u32_e32 v0, v3
	v_sub_u32_e32 v5, 0, v3
	v_rcp_iflag_f32_e32 v0, v0
	s_nop 1
	global_atomic_add v4, v1, v225, s[14:15] sc0
	v_mul_f32_e32 v0, 0x4f7ffffe, v0
	v_cvt_u32_f32_e32 v0, v0
	v_mul_lo_u32 v5, v5, v0
	v_mul_hi_u32 v5, v0, v5
	v_add_u32_e32 v0, v0, v5
	s_waitcnt vmcnt(0)
	v_mul_hi_u32 v0, v4, v0
	v_mul_lo_u32 v5, v0, v3
	v_sub_u32_e32 v5, v4, v5
	v_add_u32_e32 v6, 1, v0
	v_cmp_ge_u32_e32 vcc, v5, v3
	v_add_u32_e32 v4, 1, v4
	s_nop 0
	v_cndmask_b32_e32 v0, v0, v6, vcc
	v_sub_u32_e32 v6, v5, v3
	v_cndmask_b32_e32 v5, v5, v6, vcc
	v_add_u32_e32 v6, 1, v0
	v_cmp_ge_u32_e32 vcc, v5, v3
	s_nop 1
	v_cndmask_b32_e32 v0, v0, v6, vcc
	v_mul_lo_u32 v5, v3, v0
	v_add_u32_e32 v3, v5, v3
	v_cmp_ne_u32_e32 vcc, v4, v3
	s_and_saveexec_b64 s[14:15], vcc
	s_xor_b64 s[14:15], exec, s[14:15]
	s_cbranch_execz .LBB0_1033
	buffer_inv sc1
	v_readlane_b32 s16, v250, 33
	v_readlane_b32 s17, v250, 34
	s_waitcnt lgkmcnt(0)
	s_nop 3
	global_load_dword v2, v1, s[16:17] sc1
	s_waitcnt vmcnt(0)
	v_cmp_eq_u32_e32 vcc, v2, v0
	s_and_saveexec_b64 s[16:17], vcc
	s_cbranch_execz .LBB0_1032
	s_mov_b32 s29, 1
	s_mov_b64 s[30:31], 0
	s_branch .LBB0_1023

.LBB0_2079:
	s_mov_b32 s0, -1
	s_waitcnt vmcnt(0)
	s_waitcnt vmcnt(0) lgkmcnt(0)
	v_mbcnt_lo_u32_b32 v0, s0, 0
	v_mbcnt_hi_u32_b32 v0, s0, v0
	v_readlane_b32 s0, v250, 30
	s_barrier
	s_nop 0
	v_cmp_eq_u32_e32 vcc, s0, v0
	s_and_saveexec_b64 s[0:1], vcc
	s_cbranch_execz .LBB0_2095
	v_readlane_b32 s14, v250, 8
	s_waitcnt vmcnt(0) expcnt(0) lgkmcnt(0)
	s_mov_b64 s[16:17], -1
	v_mov_b32_e32 v0, s14
	v_readlane_b32 s14, v250, 31
	v_readlane_b32 s15, v250, 32
	ds_read_b32 v2, v0
	s_waitcnt lgkmcnt(0)
	v_cvt_f32_u32_e32 v0, v2
	s_nop 1
	global_atomic_add v3, v1, v225, s[14:15] sc0
	v_sub_u32_e32 v4, 0, v2
	v_readlane_b32 s14, v250, 33
	v_rcp_iflag_f32_e32 v0, v0
	v_readlane_b32 s15, v250, 34
	v_mul_f32_e32 v0, 0x4f7ffffe, v0
	v_cvt_u32_f32_e32 v0, v0
	v_mul_lo_u32 v4, v4, v0
	v_mul_hi_u32 v4, v0, v4
	v_add_u32_e32 v0, v0, v4
	s_waitcnt vmcnt(0)
	buffer_inv sc1
	v_mul_hi_u32 v0, v3, v0
	v_mul_lo_u32 v4, v0, v2
	v_sub_u32_e32 v4, v3, v4
	v_cmp_ge_u32_e32 vcc, v4, v2
	v_add_u32_e32 v5, 1, v0
	v_add_u32_e32 v3, 1, v3
	v_cndmask_b32_e32 v0, v0, v5, vcc
	v_sub_u32_e32 v5, v4, v2
	v_cndmask_b32_e32 v4, v4, v5, vcc
	v_cmp_ge_u32_e32 vcc, v4, v2
	v_add_u32_e32 v4, 1, v0
	s_nop 0
	v_cndmask_b32_e32 v0, v0, v4, vcc
	v_mul_lo_u32 v4, v2, v0
	v_add_u32_e32 v2, v4, v2
	v_cmp_ne_u32_e32 vcc, v3, v2
	v_mov_b64_e32 v[2:3], s[14:15]
	s_and_saveexec_b64 s[14:15], vcc
	s_cbranch_execz .LBB0_2092
	v_readlane_b32 s16, v250, 33
	v_readlane_b32 s17, v250, 34
	s_mov_b64 s[30:31], 0
	s_nop 3
	global_load_dword v2, v1, s[16:17] sc1
	s_waitcnt vmcnt(0)
	v_cmp_eq_u32_e32 vcc, v2, v0
	s_and_saveexec_b64 s[16:17], vcc
	s_cbranch_execz .LBB0_2091
	s_mov_b32 s29, 1
	s_branch .LBB0_2084

.LBB0_2094:
	s_or_b64 exec, exec, s[14:15]
	s_waitcnt vmcnt(0)
	s_waitcnt vmcnt(0)
